# dense gate/up GEMM: per-tile epilogue alignment barriers removed (only the last tile keeps the wr==0 barrier), so one wave group's epilogue overlaps the other's last MMA segment
# speedup vs baseline: 1.0001x; 1.0001x over previous
; #define PG8_STAGE(bufoff, gbase, voff) do { _Pragma("unroll") for (int _i = 0; _i < 2; ++_i) \
;         __builtin_amdgcn_global_load_lds((const unsigned*)((const char*)(gbase) + (voff)[_i]), (LAS unsigned*)(lds + (bufoff) + ldsw + _i * 8192), 16, 0, 0); } while (0)
; #define PG8_LDA(dst, b, h) do { _Pragma("unroll") for (int m = 0; m < 4; ++m) dst[m] = PG8_LD32(lds + PG8_SA(b, h) + aoff + m * 2048); } while (0)
; #define PG8_LDB(dst, b, h) do { _Pragma("unroll") for (int n = 0; n < 2; ++n) dst[n] = PG8_LD32(lds + PG8_SB(b, h) + boff + n * 2048); } while (0)
; #define PG8_WAIT_V(n) asm volatile("s_waitcnt vmcnt(" #n ")" ::: "memory")
; #define PG8_WAIT_L(n) asm volatile("s_waitcnt lgkmcnt(" #n ")" ::: "memory")
; #define PG8_BAR __builtin_amdgcn_s_barrier()
; #define PG8_SCHED __builtin_amdgcn_sched_barrier(0)
; #define PG8_STA(bufoff, nextflag, h, koff) do { if constexpr (Sched::GATHER) { unsigned _o[2]; _o[0] = (nextflag) ? nxtA[h][0] : curA[h][0]; _o[1] = (nextflag) ? nxtA[h][1] : curA[h][1]; PG8_STAGE(bufoff, Ab + (koff), _o); } \
;         else { PG8_STAGE(bufoff, ((nextflag) ? nA : cA) + (size_t)(h) * hstep + (koff), voffA); } } while (0)
; template <class Epi, class Sched, bool ALIGN_EPI, int DT>
; __device__ __forceinline__ void gemm_phase(LAS unsigned char* lds, const int KB, const Sched& S, const Epi& E) {
;     ...
;             PG8_LDB(B0, 0, 0); PG8_LDB(B1, 0, 1); PG8_SCHED; PG8_LDA(At, 0, 0); PG8_STA(PG8_SA(1, 1), false, 1, k1);
;             PG8_WAIT_V(8); PG8_WAIT_L(0); PG8_BAR; PG8_MMA(0, 0, At, B0); PG8_MMA(0, 1, At, B1); PG8_BAR; PG8_SCHED;
;             PG8_LDA(At, 0, 1); PG8_STAGE(PG8_SB(0, 0), b2, voffB); PG8_STAGE(PG8_SB(0, 1), b2 + hstep, voffB); PG8_STA(PG8_SA(0, 0), last, 0, k2);
;             PG8_WAIT_V(8); PG8_WAIT_L(0); PG8_BAR; PG8_MMA(1, 0, At, B0); PG8_MMA(1, 1, At, B1); PG8_BAR; PG8_SCHED;
.LBB0_1154:
	ds_read_b128 v[70:73], v167
	ds_read_b128 v[156:159], v167 offset:1024
	ds_read_b128 v[160:163], v167 offset:2048
	ds_read_b128 v[172:175], v167 offset:3072
	ds_read_b128 v[176:179], v168
	ds_read_b128 v[180:183], v168 offset:1024
	ds_read_b128 v[184:187], v168 offset:2048
	ds_read_b128 v[188:191], v168 offset:3072
	s_add_u32 s30, s28, 0x100
	s_addc_u32 s31, s29, 0
	s_add_u32 s63, s56, s28
	s_addc_u32 s66, s57, s29
	s_cmp_eq_u32 s62, 12
	s_cselect_b64 s[36:37], -1, 0
	s_and_b64 s[34:35], s[36:37], exec
	s_cselect_b32 s67, 0, s30
	s_cselect_b32 s35, s17, s66
	s_cselect_b32 s34, s19, s63
	v_lshl_add_u64 v[192:193], v[66:67], 0, s[28:29]
	s_add_i32 m0, s25, 0xc000
	ds_read_b128 v[196:199], v169
	ds_read_b128 v[200:203], v169 offset:1024
	ds_read_b128 v[204:207], v169 offset:2048
	ds_read_b128 v[208:211], v169 offset:3072
	ds_read_b128 v[212:215], v169 offset:4096
	ds_read_b128 v[216:219], v169 offset:5120
	ds_read_b128 v[220:223], v169 offset:6144
	ds_read_b128 v[224:227], v169 offset:7168
	global_load_lds_dwordx4 v[192:193], off
	v_lshl_add_u64 v[192:193], v[68:69], 0, s[28:29]
	s_add_i32 m0, s25, 0xe000
	s_nop 0
	global_load_lds_dwordx4 v[192:193], off
	s_waitcnt vmcnt(8)
	s_waitcnt lgkmcnt(0)
	s_barrier
	s_setprio 1
	s_waitcnt lgkmcnt(0)
	v_mfma_i32_16x16x64_i8 v[134:137], v[70:73], v[196:199], v[134:137]
	v_mfma_i32_16x16x64_i8 v[126:129], v[160:163], v[196:199], v[126:129]
	v_mfma_i32_16x16x64_i8 v[118:121], v[70:73], v[204:207], v[118:121]
	v_mfma_i32_16x16x64_i8 v[110:113], v[160:163], v[204:207], v[110:113]
	v_mfma_i32_16x16x64_i8 v[102:105], v[70:73], v[212:215], v[102:105]
	v_mfma_i32_16x16x64_i8 v[94:97], v[160:163], v[212:215], v[94:97]
	v_mfma_i32_16x16x64_i8 v[86:89], v[70:73], v[220:223], v[86:89]
	v_mfma_i32_16x16x64_i8 v[78:81], v[160:163], v[220:223], v[78:81]
	v_mfma_i32_16x16x64_i8 v[134:137], v[156:159], v[200:203], v[134:137]
	v_mfma_i32_16x16x64_i8 v[126:129], v[172:175], v[200:203], v[126:129]
	v_mfma_i32_16x16x64_i8 v[118:121], v[156:159], v[208:211], v[118:121]
	v_mfma_i32_16x16x64_i8 v[110:113], v[172:175], v[208:211], v[110:113]
	v_mfma_i32_16x16x64_i8 v[102:105], v[156:159], v[216:219], v[102:105]
	v_mfma_i32_16x16x64_i8 v[94:97], v[172:175], v[216:219], v[94:97]
	v_mfma_i32_16x16x64_i8 v[86:89], v[156:159], v[224:227], v[86:89]
	v_mfma_i32_16x16x64_i8 v[78:81], v[172:175], v[224:227], v[78:81]
	s_setprio 0
	s_setprio 1
	v_mfma_i32_16x16x64_i8 v[130:133], v[176:179], v[196:199], v[130:133]
	v_mfma_i32_16x16x64_i8 v[122:125], v[184:187], v[196:199], v[122:125]
	v_mfma_i32_16x16x64_i8 v[114:117], v[176:179], v[204:207], v[114:117]
	v_mfma_i32_16x16x64_i8 v[106:109], v[184:187], v[204:207], v[106:109]
	v_mfma_i32_16x16x64_i8 v[98:101], v[176:179], v[212:215], v[98:101]
	v_mfma_i32_16x16x64_i8 v[90:93], v[184:187], v[212:215], v[90:93]
	v_mfma_i32_16x16x64_i8 v[82:85], v[176:179], v[220:223], v[82:85]
	v_mfma_i32_16x16x64_i8 v[74:77], v[184:187], v[220:223], v[74:77]
	v_mfma_i32_16x16x64_i8 v[130:133], v[180:183], v[200:203], v[130:133]
	v_mfma_i32_16x16x64_i8 v[122:125], v[188:191], v[200:203], v[122:125]
	v_mfma_i32_16x16x64_i8 v[114:117], v[180:183], v[208:211], v[114:117]
	v_mfma_i32_16x16x64_i8 v[106:109], v[188:191], v[208:211], v[106:109]
	v_mfma_i32_16x16x64_i8 v[98:101], v[180:183], v[216:219], v[98:101]
	v_mfma_i32_16x16x64_i8 v[90:93], v[188:191], v[216:219], v[90:93]
	v_mfma_i32_16x16x64_i8 v[82:85], v[180:183], v[224:227], v[82:85]
	v_mfma_i32_16x16x64_i8 v[74:77], v[188:191], v[224:227], v[74:77]
	s_setprio 0
	s_barrier
	s_add_i32 s28, s49, s38
	v_lshl_add_u64 v[192:193], s[34:35], 0, v[140:141]
	s_mov_b32 m0, s28
	ds_read_b128 v[196:199], v169 offset:16384
	ds_read_b128 v[200:203], v169 offset:17408
	ds_read_b128 v[204:207], v169 offset:18432
	ds_read_b128 v[208:211], v169 offset:19456
	ds_read_b128 v[212:215], v169 offset:20480
	ds_read_b128 v[216:219], v169 offset:21504
	ds_read_b128 v[220:223], v169 offset:22528
	ds_read_b128 v[224:227], v169 offset:23552
	global_load_lds_dwordx4 v[192:193], off
	s_add_i32 m0, s28, 0x2000
	s_add_u32 s28, s34, 0x40000
	v_lshl_add_u64 v[228:229], s[34:35], 0, v[138:139]
	s_addc_u32 s29, s35, 0
	s_add_i32 s63, s52, s38
	global_load_lds_dwordx4 v[228:229], off
	v_lshl_add_u64 v[230:231], s[28:29], 0, v[140:141]
	s_mov_b32 m0, s63
	s_nop 0
	global_load_lds_dwordx4 v[230:231], off
	v_lshl_add_u64 v[230:231], s[28:29], 0, v[138:139]
	s_add_i32 m0, s63, 0x2000
	s_and_b64 s[28:29], s[6:7], s[36:37]
	s_and_b64 s[28:29], s[28:29], exec
	s_cselect_b32 s28, s20, s26
	s_cselect_b32 s29, s21, s27
	s_add_u32 s28, s28, s67
	s_addc_u32 s29, s29, 0
	global_load_lds_dwordx4 v[230:231], off
	v_lshl_add_u64 v[230:231], s[28:29], 0, v[142:143]
	s_mov_b32 m0, s25
	v_lshl_add_u64 v[232:233], s[28:29], 0, v[144:145]
	global_load_lds_dwordx4 v[230:231], off
	s_mov_b32 m0, s41
	s_nop 0
	global_load_lds_dwordx4 v[232:233], off
	s_waitcnt vmcnt(8)
	s_waitcnt lgkmcnt(0)
	s_barrier
; #define PG8_LDA(dst, b, h) do { _Pragma("unroll") for (int m = 0; m < 4; ++m) dst[m] = PG8_LD32(lds + PG8_SA(b, h) + aoff + m * 2048); } while (0)
; #define PG8_LDB(dst, b, h) do { _Pragma("unroll") for (int n = 0; n < 2; ++n) dst[n] = PG8_LD32(lds + PG8_SB(b, h) + boff + n * 2048); } while (0)
; #define PG8_WAIT_V(n) asm volatile("s_waitcnt vmcnt(" #n ")" ::: "memory")
; #define PG8_WAIT_L(n) asm volatile("s_waitcnt lgkmcnt(" #n ")" ::: "memory")
; #define PG8_BAR __builtin_amdgcn_s_barrier()
; #define PG8_SCHED __builtin_amdgcn_sched_barrier(0)
; #define PG8_STA(bufoff, nextflag, h, koff) do { if constexpr (Sched::GATHER) { unsigned _o[2]; _o[0] = (nextflag) ? nxtA[h][0] : curA[h][0]; _o[1] = (nextflag) ? nxtA[h][1] : curA[h][1]; PG8_STAGE(bufoff, Ab + (koff), _o); } \
;         else { PG8_STAGE(bufoff, ((nextflag) ? nA : cA) + (size_t)(h) * hstep + (koff), voffA); } } while (0)
; template <class Epi, class Sched, bool ALIGN_EPI, int DT>
; __device__ __forceinline__ void gemm_phase(LAS unsigned char* lds, const int KB, const Sched& S, const Epi& E) {
;     ...
;             PG8_WAIT_V(8); PG8_WAIT_L(0); PG8_BAR; PG8_MMA(1, 0, At, B0); PG8_MMA(1, 1, At, B1); PG8_BAR; PG8_SCHED;
;             PG8_LDB(B0, 1, 0); PG8_LDB(B1, 1, 1); PG8_SCHED; PG8_LDA(At, 1, 0); PG8_STA(PG8_SA(0, 1), last, 1, k2);
;             PG8_WAIT_V(8); PG8_WAIT_L(0); PG8_BAR; PG8_MMA(0, 0, At, B0); PG8_MMA(0, 1, At, B1); PG8_BAR; PG8_SCHED;
	s_setprio 1
	s_waitcnt lgkmcnt(0)
	v_mfma_i32_16x16x64_i8 v[62:65], v[70:73], v[196:199], v[62:65]
	v_mfma_i32_16x16x64_i8 v[54:57], v[160:163], v[196:199], v[54:57]
	v_mfma_i32_16x16x64_i8 v[46:49], v[70:73], v[204:207], v[46:49]
	v_mfma_i32_16x16x64_i8 v[38:41], v[160:163], v[204:207], v[38:41]
	v_mfma_i32_16x16x64_i8 v[30:33], v[70:73], v[212:215], v[30:33]
	v_mfma_i32_16x16x64_i8 v[22:25], v[160:163], v[212:215], v[22:25]
	v_mfma_i32_16x16x64_i8 v[6:9], v[70:73], v[220:223], v[6:9]
	v_mfma_i32_16x16x64_i8 v[2:5], v[160:163], v[220:223], v[2:5]
	v_mfma_i32_16x16x64_i8 v[62:65], v[156:159], v[200:203], v[62:65]
	v_mfma_i32_16x16x64_i8 v[54:57], v[172:175], v[200:203], v[54:57]
	v_mfma_i32_16x16x64_i8 v[46:49], v[156:159], v[208:211], v[46:49]
	v_mfma_i32_16x16x64_i8 v[38:41], v[172:175], v[208:211], v[38:41]
	v_mfma_i32_16x16x64_i8 v[30:33], v[156:159], v[216:219], v[30:33]
	v_mfma_i32_16x16x64_i8 v[22:25], v[172:175], v[216:219], v[22:25]
	v_mfma_i32_16x16x64_i8 v[6:9], v[156:159], v[224:227], v[6:9]
	v_mfma_i32_16x16x64_i8 v[2:5], v[172:175], v[224:227], v[2:5]
	s_setprio 0
	s_setprio 1
	v_mfma_i32_16x16x64_i8 v[58:61], v[176:179], v[196:199], v[58:61]
	v_mfma_i32_16x16x64_i8 v[50:53], v[184:187], v[196:199], v[50:53]
	v_mfma_i32_16x16x64_i8 v[42:45], v[176:179], v[204:207], v[42:45]
	v_mfma_i32_16x16x64_i8 v[34:37], v[184:187], v[204:207], v[34:37]
	v_mfma_i32_16x16x64_i8 v[26:29], v[176:179], v[212:215], v[26:29]
	v_mfma_i32_16x16x64_i8 v[18:21], v[184:187], v[212:215], v[18:21]
	v_mfma_i32_16x16x64_i8 v[14:17], v[176:179], v[220:223], v[14:17]
	v_mfma_i32_16x16x64_i8 v[10:13], v[184:187], v[220:223], v[10:13]
	v_mfma_i32_16x16x64_i8 v[58:61], v[180:183], v[200:203], v[58:61]
	v_mfma_i32_16x16x64_i8 v[50:53], v[188:191], v[200:203], v[50:53]
	v_mfma_i32_16x16x64_i8 v[42:45], v[180:183], v[208:211], v[42:45]
	v_mfma_i32_16x16x64_i8 v[34:37], v[188:191], v[208:211], v[34:37]
	v_mfma_i32_16x16x64_i8 v[26:29], v[180:183], v[216:219], v[26:29]
	v_mfma_i32_16x16x64_i8 v[18:21], v[188:191], v[216:219], v[18:21]
	v_mfma_i32_16x16x64_i8 v[14:17], v[180:183], v[224:227], v[14:17]
	v_mfma_i32_16x16x64_i8 v[10:13], v[188:191], v[224:227], v[10:13]
	s_setprio 0
	s_barrier
	s_add_i32 s36, 0, 0x18000
	v_add_u32_e32 v1, s36, v165
	s_add_i32 s37, 0, 0x1c000
	ds_read_b128 v[70:73], v1
	ds_read_b128 v[156:159], v1 offset:1024
	ds_read_b128 v[160:163], v1 offset:2048
	ds_read_b128 v[172:175], v1 offset:3072
	v_add_u32_e32 v1, s37, v165
	ds_read_b128 v[176:179], v1
	ds_read_b128 v[180:183], v1 offset:1024
	ds_read_b128 v[184:187], v1 offset:2048
	ds_read_b128 v[188:191], v1 offset:3072
	s_add_u32 s28, s28, 0x40000
	s_addc_u32 s29, s29, 0
	s_mov_b32 m0, s42
	v_lshl_add_u64 v[234:235], s[28:29], 0, v[142:143]
	ds_read_b128 v[196:199], v169 offset:32768
	ds_read_b128 v[200:203], v169 offset:33792
	ds_read_b128 v[204:207], v169 offset:34816
	ds_read_b128 v[208:211], v169 offset:35840
	ds_read_b128 v[212:215], v169 offset:36864
	ds_read_b128 v[216:219], v169 offset:37888
	ds_read_b128 v[220:223], v169 offset:38912
	ds_read_b128 v[224:227], v169 offset:39936
	global_load_lds_dwordx4 v[234:235], off
	v_lshl_add_u64 v[234:235], s[28:29], 0, v[144:145]
	s_mov_b32 m0, s43
	s_nop 0
	global_load_lds_dwordx4 v[234:235], off
	s_waitcnt vmcnt(8)
	s_waitcnt lgkmcnt(0)
	s_barrier
	s_setprio 1
	s_waitcnt lgkmcnt(0)
	v_mfma_i32_16x16x64_i8 v[134:137], v[70:73], v[196:199], v[134:137]
	v_mfma_i32_16x16x64_i8 v[126:129], v[160:163], v[196:199], v[126:129]
	v_mfma_i32_16x16x64_i8 v[118:121], v[70:73], v[204:207], v[118:121]
	v_mfma_i32_16x16x64_i8 v[110:113], v[160:163], v[204:207], v[110:113]
	v_mfma_i32_16x16x64_i8 v[102:105], v[70:73], v[212:215], v[102:105]
	v_mfma_i32_16x16x64_i8 v[94:97], v[160:163], v[212:215], v[94:97]
	v_mfma_i32_16x16x64_i8 v[86:89], v[70:73], v[220:223], v[86:89]
	v_mfma_i32_16x16x64_i8 v[78:81], v[160:163], v[220:223], v[78:81]
	v_mfma_i32_16x16x64_i8 v[134:137], v[156:159], v[200:203], v[134:137]
	v_mfma_i32_16x16x64_i8 v[126:129], v[172:175], v[200:203], v[126:129]
	v_mfma_i32_16x16x64_i8 v[118:121], v[156:159], v[208:211], v[118:121]
	v_mfma_i32_16x16x64_i8 v[110:113], v[172:175], v[208:211], v[110:113]
	v_mfma_i32_16x16x64_i8 v[102:105], v[156:159], v[216:219], v[102:105]
	v_mfma_i32_16x16x64_i8 v[94:97], v[172:175], v[216:219], v[94:97]
	v_mfma_i32_16x16x64_i8 v[86:89], v[156:159], v[224:227], v[86:89]
	v_mfma_i32_16x16x64_i8 v[78:81], v[172:175], v[224:227], v[78:81]
	s_setprio 0
	s_setprio 1
	v_mfma_i32_16x16x64_i8 v[130:133], v[176:179], v[196:199], v[130:133]
	v_mfma_i32_16x16x64_i8 v[122:125], v[184:187], v[196:199], v[122:125]
	v_mfma_i32_16x16x64_i8 v[114:117], v[176:179], v[204:207], v[114:117]
	v_mfma_i32_16x16x64_i8 v[106:109], v[184:187], v[204:207], v[106:109]
	v_mfma_i32_16x16x64_i8 v[98:101], v[176:179], v[212:215], v[98:101]
	v_mfma_i32_16x16x64_i8 v[90:93], v[184:187], v[212:215], v[90:93]
	v_mfma_i32_16x16x64_i8 v[82:85], v[176:179], v[220:223], v[82:85]
	v_mfma_i32_16x16x64_i8 v[74:77], v[184:187], v[220:223], v[74:77]
	v_mfma_i32_16x16x64_i8 v[130:133], v[180:183], v[200:203], v[130:133]
	v_mfma_i32_16x16x64_i8 v[122:125], v[188:191], v[200:203], v[122:125]
	v_mfma_i32_16x16x64_i8 v[114:117], v[180:183], v[208:211], v[114:117]
	v_mfma_i32_16x16x64_i8 v[106:109], v[188:191], v[208:211], v[106:109]
	v_mfma_i32_16x16x64_i8 v[98:101], v[180:183], v[216:219], v[98:101]
	v_mfma_i32_16x16x64_i8 v[90:93], v[188:191], v[216:219], v[90:93]
	v_mfma_i32_16x16x64_i8 v[82:85], v[180:183], v[224:227], v[82:85]
	v_mfma_i32_16x16x64_i8 v[74:77], v[188:191], v[224:227], v[74:77]
	s_setprio 0
	s_barrier
; #define PG8_STAGE(bufoff, gbase, voff) do { _Pragma("unroll") for (int _i = 0; _i < 2; ++_i) \
;         __builtin_amdgcn_global_load_lds((const unsigned*)((const char*)(gbase) + (voff)[_i]), (LAS unsigned*)(lds + (bufoff) + ldsw + _i * 8192), 16, 0, 0); } while (0)
; #define PG8_WAIT_V(n) asm volatile("s_waitcnt vmcnt(" #n ")" ::: "memory")
; #define PG8_BAR __builtin_amdgcn_s_barrier()
;     __device__ __forceinline__ void operator()(const f32x4 (&acc)[2][2][4][2], const Unit& u, int wr, int wc, int fr, int fq) const {
;         const int row0 = u.pm * BM + wr * 64 + fr, col0 = u.pn * HALF + wc * 32 + 8 * fq;
;         const float* cm = colmax + (size_t)u.e * 2 * ldc + u.pn * BM + wc * 32 + 8 * fq;
;         const f32x4 cg0 = *(const f32x4*)(cm), cg1 = *(const f32x4*)(cm + 4), cu0 = *(const f32x4*)(cm + HALF), cu1 = *(const f32x4*)(cm + HALF + 4);
;         const float cg[8] = {cg0[0], cg0[1], cg0[2], cg0[3], cg1[0], cg1[1], cg1[2], cg1[3]}, cu[8] = {cu0[0], cu0[1], cu0[2], cu0[3], cu1[0], cu1[1], cu1[2], cu1[3]};
;         int cume = 0, cnte = 0x7fffffff; if (rowidx) { cume = tab[8 + u.e]; cnte = tab[u.e]; }
; #pragma unroll
;         for (int ai = 0; ai < 2; ++ai)
; #pragma unroll
;             for (int m = 0; m < 4; ++m) { const int r = row0 + ai * HALF + m * 16; unsigned char* rowp = O + (size_t)r * ldc + col0;
;                 float sa; if (rowidx) { const int rl = r - cume * BM; sa = (rl < cnte) ? rowmax[u.e * ECAP + rl] : 0.f; } else sa = rowmax[r];
;                 sa *= (1.f / (127.f * 127.f));
;                 float o[8];
; #pragma unroll
;                 for (int n = 0; n < 2; ++n)
; #pragma unroll
;                     for (int j = 0; j < 4; ++j) { const float g = (float)__builtin_bit_cast(i32x4, acc[ai][0][m][n])[j] * (sa * cg[n * 4 + j]), up = (float)__builtin_bit_cast(i32x4, acc[ai][1][m][n])[j] * (sa * cu[n * 4 + j]);
; template <class Epi, class Sched, bool ALIGN_EPI, int DT>
; __device__ __forceinline__ void gemm_phase(LAS unsigned char* lds, const int KB, const Sched& S, const Epi& E) {
;     ...
;             PG8_LDA(At, 1, 1); PG8_STAGE(PG8_SB(1, 0), b3, voffB); PG8_STAGE(PG8_SB(1, 1), b3 + hstep, voffB); PG8_STA(PG8_SA(1, 0), last, 0, k3);
;             PG8_WAIT_V(8); PG8_WAIT_L(0); PG8_BAR; PG8_MMA(1, 0, At, B0); PG8_MMA(1, 1, At, B1); PG8_BAR; PG8_SCHED;
;         }
;         if constexpr (ALIGN_EPI) { if (wr == 0) PG8_BAR; }
	s_add_i32 s28, s36, s38
	v_lshl_add_u64 v[192:193], v[192:193], 0, s[12:13]
	s_mov_b32 m0, s28
	ds_read_b128 v[196:199], v169 offset:49152
	ds_read_b128 v[200:203], v169 offset:50176
	ds_read_b128 v[204:207], v169 offset:51200
	ds_read_b128 v[208:211], v169 offset:52224
	ds_read_b128 v[212:215], v169 offset:53248
	ds_read_b128 v[216:219], v169 offset:54272
	ds_read_b128 v[220:223], v169 offset:55296
	ds_read_b128 v[224:227], v169 offset:56320
	global_load_lds_dwordx4 v[192:193], off
	s_add_i32 m0, s28, 0x2000
	s_add_u32 s28, s34, 0x40080
	v_lshl_add_u64 v[192:193], v[228:229], 0, s[12:13]
	s_addc_u32 s29, s35, 0
	s_add_i32 s34, s37, s38
	global_load_lds_dwordx4 v[192:193], off
	v_lshl_add_u64 v[192:193], s[28:29], 0, v[140:141]
	s_mov_b32 m0, s34
	s_nop 0
	global_load_lds_dwordx4 v[192:193], off
	v_lshl_add_u64 v[192:193], s[28:29], 0, v[138:139]
	s_add_i32 m0, s34, 0x2000
	s_nop 0
	global_load_lds_dwordx4 v[192:193], off
	v_lshl_add_u64 v[192:193], v[230:231], 0, s[12:13]
	s_mov_b32 m0, s45
	s_nop 0
	global_load_lds_dwordx4 v[192:193], off
	v_lshl_add_u64 v[192:193], v[232:233], 0, s[12:13]
	s_mov_b32 m0, s46
	s_nop 0
	global_load_lds_dwordx4 v[192:193], off
	s_waitcnt vmcnt(8)
	s_waitcnt lgkmcnt(0)
	s_barrier
	s_setprio 1
	s_waitcnt lgkmcnt(0)
	v_mfma_i32_16x16x64_i8 v[62:65], v[70:73], v[196:199], v[62:65]
	v_mfma_i32_16x16x64_i8 v[54:57], v[160:163], v[196:199], v[54:57]
	v_mfma_i32_16x16x64_i8 v[46:49], v[70:73], v[204:207], v[46:49]
	v_mfma_i32_16x16x64_i8 v[38:41], v[160:163], v[204:207], v[38:41]
	v_mfma_i32_16x16x64_i8 v[30:33], v[70:73], v[212:215], v[30:33]
	v_mfma_i32_16x16x64_i8 v[22:25], v[160:163], v[212:215], v[22:25]
	v_mfma_i32_16x16x64_i8 v[6:9], v[70:73], v[220:223], v[6:9]
	v_mfma_i32_16x16x64_i8 v[2:5], v[160:163], v[220:223], v[2:5]
	v_mfma_i32_16x16x64_i8 v[62:65], v[156:159], v[200:203], v[62:65]
	v_mfma_i32_16x16x64_i8 v[54:57], v[172:175], v[200:203], v[54:57]
	v_mfma_i32_16x16x64_i8 v[46:49], v[156:159], v[208:211], v[46:49]
	v_mfma_i32_16x16x64_i8 v[38:41], v[172:175], v[208:211], v[38:41]
	v_mfma_i32_16x16x64_i8 v[30:33], v[156:159], v[216:219], v[30:33]
	v_mfma_i32_16x16x64_i8 v[22:25], v[172:175], v[216:219], v[22:25]
	v_mfma_i32_16x16x64_i8 v[6:9], v[156:159], v[224:227], v[6:9]
	v_mfma_i32_16x16x64_i8 v[2:5], v[172:175], v[224:227], v[2:5]
	s_setprio 0
	s_setprio 1
	v_mfma_i32_16x16x64_i8 v[58:61], v[176:179], v[196:199], v[58:61]
	v_mfma_i32_16x16x64_i8 v[50:53], v[184:187], v[196:199], v[50:53]
	v_mfma_i32_16x16x64_i8 v[42:45], v[176:179], v[204:207], v[42:45]
	v_mfma_i32_16x16x64_i8 v[34:37], v[184:187], v[204:207], v[34:37]
	v_mfma_i32_16x16x64_i8 v[26:29], v[176:179], v[212:215], v[26:29]
	v_mfma_i32_16x16x64_i8 v[18:21], v[184:187], v[212:215], v[18:21]
	v_mfma_i32_16x16x64_i8 v[14:17], v[176:179], v[220:223], v[14:17]
	v_mfma_i32_16x16x64_i8 v[10:13], v[184:187], v[220:223], v[10:13]
	v_mfma_i32_16x16x64_i8 v[58:61], v[180:183], v[200:203], v[58:61]
	v_mfma_i32_16x16x64_i8 v[50:53], v[188:191], v[200:203], v[50:53]
	v_mfma_i32_16x16x64_i8 v[42:45], v[180:183], v[208:211], v[42:45]
	v_mfma_i32_16x16x64_i8 v[34:37], v[188:191], v[208:211], v[34:37]
	v_mfma_i32_16x16x64_i8 v[26:29], v[180:183], v[216:219], v[26:29]
	v_mfma_i32_16x16x64_i8 v[18:21], v[188:191], v[216:219], v[18:21]
	v_mfma_i32_16x16x64_i8 v[14:17], v[180:183], v[224:227], v[14:17]
	v_mfma_i32_16x16x64_i8 v[10:13], v[188:191], v[224:227], v[10:13]
	s_setprio 0
	s_barrier
	s_add_i32 s62, s62, 2
	s_cmp_gt_u32 s62, 13
	s_mov_b64 s[28:29], s[30:31]
	s_cbranch_scc0 .LBB0_1154
	s_and_b64 vcc, exec, s[14:15]
	s_cbranch_vccz .LBB0_1157
	s_and_b64 vcc, exec, s[6:7]
	s_cbranch_vccnz .LBB0_1157
	s_barrier
.LBB0_1157:
	s_lshl_b32 s26, s55, 8
	v_lshl_add_u32 v160, s24, 8, v164
	s_ashr_i32 s27, s26, 31
	v_ashrrev_i32_e32 v161, 31, v160
	v_lshl_add_u64 v[66:67], s[26:27], 2, v[146:147]
	v_lshl_add_u64 v[162:163], v[160:161], 2, s[10:11]
	global_load_dword v1, v[162:163], off
	global_load_dword v244, v[162:163], off offset:64
	global_load_dword v245, v[162:163], off offset:128
	global_load_dword v246, v[162:163], off offset:192
	global_load_dword v247, v[162:163], off offset:512
	global_load_dword v248, v[162:163], off offset:576
	global_load_dword v249, v[162:163], off offset:640
	global_load_dword v250, v[162:163], off offset:704
	global_load_dwordx4 v[172:175], v[66:67], off offset:512
	global_load_dwordx4 v[70:73], v[66:67], off
	global_load_dwordx4 v[176:179], v[66:67], off offset:528
	s_nop 0
	global_load_dwordx4 v[66:69], v[66:67], off offset:16
	v_cvt_f32_i32_e32 v181, v134
	v_cvt_f32_i32_e32 v180, v130
	v_cvt_f32_i32_e32 v135, v135
	v_cvt_f32_i32_e32 v134, v131
	v_cvt_f32_i32_e32 v131, v136
	v_cvt_f32_i32_e32 v130, v132
	v_cvt_f32_i32_e32 v136, v133
	v_cvt_f32_i32_e32 v133, v126
	v_cvt_f32_i32_e32 v132, v122
	v_cvt_f32_i32_e32 v137, v137
	v_cvt_f32_i32_e32 v183, v127
	v_cvt_f32_i32_e32 v182, v123
	v_cvt_f32_i32_e32 v184, v124
	v_cvt_f32_i32_e32 v186, v125
	v_cvt_f32_i32_e32 v185, v128
	v_cvt_f32_i32_e32 v187, v129
	v_lshl_or_b32 v156, s55, 7, v166
	v_mov_b64_e32 v[158:159], s[58:59]
	v_ashrrev_i32_e32 v157, 31, v156
	v_cvt_f32_i32_e32 v121, v121
	v_cvt_f32_i32_e32 v113, v113
	v_cvt_f32_i32_e32 v119, v119
	v_cvt_f32_i32_e32 v111, v111
	v_cvt_f32_i32_e32 v103, v103
	v_cvt_f32_i32_e32 v95, v95
	v_cvt_f32_i32_e32 v105, v105
	v_cvt_f32_i32_e32 v97, v97
	v_cvt_f32_i32_e32 v87, v87
	v_cvt_f32_i32_e32 v79, v79
	v_cvt_f32_i32_e32 v89, v89
	v_cvt_f32_i32_e32 v81, v81
	v_cvt_f32_i32_e32 v63, v63
	v_cvt_f32_i32_e32 v65, v65
	v_cvt_f32_i32_e32 v55, v55
	v_cvt_f32_i32_e32 v57, v57
	v_cvt_f32_i32_e32 v47, v47
	v_cvt_f32_i32_e32 v39, v39
	v_cvt_f32_i32_e32 v41, v41
	v_cvt_f32_i32_e32 v49, v49
	v_cvt_f32_i32_e32 v31, v31
	v_cvt_f32_i32_e32 v23, v23
	v_cvt_f32_i32_e32 v25, v25
	v_cvt_f32_i32_e32 v33, v33
	v_cvt_f32_i32_e32 v7, v7
	v_cvt_f32_i32_e32 v9, v9
	v_cvt_f32_i32_e32 v3, v3
	v_cvt_f32_i32_e32 v5, v5
	s_andn2_b64 vcc, exec, s[6:7]
	s_mov_b64 s[6:7], -1
	s_waitcnt vmcnt(0)
;     __device__ __forceinline__ void operator()(const f32x4 (&acc)[2][2][4][2], const Unit& u, int wr, int wc, int fr, int fq) const {
;     ...
;         for (int ai = 0; ai < 2; ++ai)
; #pragma unroll
;             for (int m = 0; m < 4; ++m) { const int r = row0 + ai * HALF + m * 16; unsigned char* rowp = O + (size_t)r * ldc + col0;
;                 float sa; if (rowidx) { const int rl = r - cume * BM; sa = (rl < cnte) ? rowmax[u.e * ECAP + rl] : 0.f; } else sa = rowmax[r];
;                 sa *= (1.f / (127.f * 127.f));
;                 float o[8];
; #pragma unroll
;                 for (int n = 0; n < 2; ++n)
; #pragma unroll
;                     for (int j = 0; j < 4; ++j) { const float g = (float)__builtin_bit_cast(i32x4, acc[ai][0][m][n])[j] * (sa * cg[n * 4 + j]), up = (float)__builtin_bit_cast(i32x4, acc[ai][1][m][n])[j] * (sa * cu[n * 4 + j]);
;                         o[n * 4 + j] = g * __builtin_amdgcn_rcpf(1.f + __builtin_amdgcn_exp2f(-1.4426950408889634f * g)) * up; }
;                 u32x2 w; w.x = pack_fp8x4(o[0], o[1], o[2], o[3]); w.y = pack_fp8x4(o[4], o[5], o[6], o[7]);
;                 *(u32x2*)rowp = w; }
	v_mul_f32_e32 v188, 0x38820610, v1
	v_mov_b32_e32 v122, v172
	v_mov_b32_e32 v123, v70
	v_mov_b32_e32 v70, v173
	v_mov_b32_e32 v126, v176
	v_mov_b32_e32 v127, v66
	v_mov_b32_e32 v124, v174
	v_mov_b32_e32 v125, v72
	v_mov_b32_e32 v72, v175
	v_pk_mul_f32 v[174:175], v[70:71], v[188:189] op_sel_hi:[1,0]
	v_pk_mul_f32 v[190:191], v[126:127], v[188:189] op_sel_hi:[1,0]
	v_mov_b32_e32 v66, v177
	v_pk_mul_f32 v[172:173], v[122:123], v[188:189] op_sel_hi:[1,0]
	v_pk_mul_f32 v[176:177], v[124:125], v[188:189] op_sel_hi:[1,0]
	v_pk_mul_f32 v[134:135], v[174:175], v[134:135]
	v_pk_mul_f32 v[132:133], v[190:191], v[132:133]
	v_mov_b32_e32 v128, v178
	v_mov_b32_e32 v129, v68
	v_mov_b32_e32 v68, v179
	v_pk_mul_f32 v[178:179], v[72:73], v[188:189] op_sel_hi:[1,0]
	v_pk_mul_f32 v[192:193], v[66:67], v[188:189] op_sel_hi:[1,0]
	v_pk_mul_f32 v[172:173], v[172:173], v[180:181]
	v_pk_mul_f32 v[130:131], v[176:177], v[130:131]
	v_mul_f32_e32 v161, 0xbfb8aa3b, v135
	v_mul_f32_e32 v181, 0xbfb8aa3b, v133
	v_pk_mul_f32 v[136:137], v[178:179], v[136:137]
	v_pk_mul_f32 v[174:175], v[192:193], v[182:183]
	v_mul_f32_e32 v1, 0xbfb8aa3b, v173
	v_mul_f32_e32 v171, 0xbfb8aa3b, v131
	v_exp_f32_e32 v161, v161
	v_exp_f32_e32 v181, v181
	v_mul_f32_e32 v180, 0xbfb8aa3b, v137
	v_mul_f32_e32 v182, 0xbfb8aa3b, v175
	v_exp_f32_e32 v1, v1
	v_exp_f32_e32 v171, v171
	v_exp_f32_e32 v180, v180
	v_exp_f32_e32 v182, v182
	v_pk_mul_f32 v[196:197], v[128:129], v[188:189] op_sel_hi:[1,0]
	v_pk_mul_f32 v[188:189], v[68:69], v[188:189] op_sel_hi:[1,0]
	v_pk_mul_f32 v[176:177], v[196:197], v[184:185]
	v_pk_mul_f32 v[178:179], v[188:189], v[186:187]
	v_add_f32_e32 v161, 1.0, v161
	v_add_f32_e32 v181, 1.0, v181
	v_mul_f32_e32 v183, 0xbfb8aa3b, v177
	v_mul_f32_e32 v184, 0xbfb8aa3b, v179
	v_add_f32_e32 v1, 1.0, v1
	v_add_f32_e32 v171, 1.0, v171
	v_rcp_f32_e32 v161, v161
	v_rcp_f32_e32 v181, v181
	v_exp_f32_e32 v183, v183
	v_exp_f32_e32 v184, v184
	v_add_f32_e32 v180, 1.0, v180
	v_add_f32_e32 v182, 1.0, v182
	v_rcp_f32_e32 v1, v1
	v_rcp_f32_e32 v171, v171
	v_rcp_f32_e32 v180, v180
	v_rcp_f32_e32 v182, v182
	v_mul_f32_e32 v135, v135, v161
	v_mul_f32_e32 v133, v133, v181
	v_mul_f32_e32 v1, v173, v1
	v_mul_f32_e32 v131, v131, v171
	v_mul_f32_e32 v134, v134, v135
	v_mul_f32_e32 v132, v132, v133
	v_add_f32_e32 v133, 1.0, v183
	v_add_f32_e32 v135, 1.0, v184
	v_mul_f32_e32 v137, v137, v180
	v_mul_f32_e32 v161, v175, v182
	v_mul_f32_e32 v1, v172, v1
	v_mul_f32_e32 v130, v130, v131
	v_rcp_f32_e32 v133, v133
	v_rcp_f32_e32 v135, v135
	v_mul_f32_e32 v131, v136, v137
	v_mul_f32_e32 v136, v174, v161
	v_med3_f32 v1, v1, s54, v170
	v_med3_f32 v134, v134, s54, v170
	v_med3_f32 v137, v130, s54, v170
	v_mov_b32_e32 v130, 0
	v_med3_f32 v161, v131, s54, v170
	v_cvt_pk_fp8_f32 v130, v1, v134
	v_med3_f32 v1, v132, s54, v170
	v_med3_f32 v132, v136, s54, v170
	v_mov_b32_e32 v131, 0
	v_cvt_pk_fp8_f32 v131, v1, v132
	v_mul_f32_e32 v133, v177, v133
	v_mul_f32_e32 v135, v179, v135
	v_mul_f32_e32 v133, v176, v133
	v_mul_f32_e32 v135, v178, v135
	v_med3_f32 v1, v133, s54, v170
	v_med3_f32 v132, v135, s54, v170
	v_cvt_pk_fp8_f32 v130, v137, v161 op_sel:[0,0,1]
	v_cvt_pk_fp8_f32 v131, v1, v132 op_sel:[0,0,1]
	v_mad_i64_i32 v[132:133], s[26:27], v160, s53, v[158:159]
	v_lshl_add_u64 v[132:133], v[132:133], 0, v[156:157]
	global_store_dwordx2 v[132:133], v[130:131], off
	v_or_b32_e32 v130, 16, v160
	v_ashrrev_i32_e32 v131, 31, v130
	v_lshl_add_u64 v[132:133], v[130:131], 2, s[10:11]
	v_mov_b32_e32 v1, v244
	v_cvt_f32_i32_e32 v133, v118
	v_cvt_f32_i32_e32 v132, v114
	v_cvt_f32_i32_e32 v118, v115
	v_cvt_f32_i32_e32 v115, v120
	v_cvt_f32_i32_e32 v114, v116
	v_cvt_f32_i32_e32 v120, v117
	v_cvt_f32_i32_e32 v117, v110
	v_cvt_f32_i32_e32 v116, v106
	v_cvt_f32_i32_e32 v110, v107
	v_cvt_f32_i32_e32 v107, v112
	v_cvt_f32_i32_e32 v112, v109
	v_cvt_f32_i32_e32 v106, v108
	v_mul_f32_e32 v108, 0x38820610, v1
	v_pk_mul_f32 v[172:173], v[124:125], v[108:109] op_sel_hi:[1,0]
	v_pk_mul_f32 v[174:175], v[72:73], v[108:109] op_sel_hi:[1,0]
	v_pk_mul_f32 v[176:177], v[126:127], v[108:109] op_sel_hi:[1,0]
	v_pk_mul_f32 v[134:135], v[122:123], v[108:109] op_sel_hi:[1,0]
	v_pk_mul_f32 v[136:137], v[70:71], v[108:109] op_sel_hi:[1,0]
	v_pk_mul_f32 v[178:179], v[66:67], v[108:109] op_sel_hi:[1,0]
	v_pk_mul_f32 v[180:181], v[128:129], v[108:109] op_sel_hi:[1,0]
	v_pk_mul_f32 v[108:109], v[68:69], v[108:109] op_sel_hi:[1,0]
	v_pk_mul_f32 v[114:115], v[172:173], v[114:115]
	v_pk_mul_f32 v[120:121], v[174:175], v[120:121]
	v_pk_mul_f32 v[116:117], v[176:177], v[116:117]
	v_pk_mul_f32 v[132:133], v[134:135], v[132:133]
	v_pk_mul_f32 v[108:109], v[108:109], v[112:113]
	v_mul_f32_e32 v113, 0xbfb8aa3b, v115
	v_mul_f32_e32 v131, 0xbfb8aa3b, v121
	v_mul_f32_e32 v134, 0xbfb8aa3b, v117
	v_exp_f32_e32 v113, v113
	v_exp_f32_e32 v131, v131
	v_exp_f32_e32 v134, v134
	v_pk_mul_f32 v[118:119], v[136:137], v[118:119]
	v_pk_mul_f32 v[110:111], v[178:179], v[110:111]
	v_pk_mul_f32 v[106:107], v[180:181], v[106:107]
	v_mul_f32_e32 v1, 0xbfb8aa3b, v133
	v_mul_f32_e32 v112, 0xbfb8aa3b, v119
	v_mul_f32_e32 v135, 0xbfb8aa3b, v111
	v_mul_f32_e32 v136, 0xbfb8aa3b, v107
	v_add_f32_e32 v113, 1.0, v113
	v_add_f32_e32 v131, 1.0, v131
	v_add_f32_e32 v134, 1.0, v134
	v_mul_f32_e32 v137, 0xbfb8aa3b, v109
	v_exp_f32_e32 v1, v1
	v_exp_f32_e32 v112, v112
	v_exp_f32_e32 v135, v135
	v_exp_f32_e32 v136, v136
	v_rcp_f32_e32 v113, v113
	v_rcp_f32_e32 v131, v131
	v_rcp_f32_e32 v134, v134
	v_exp_f32_e32 v137, v137
	v_add_f32_e32 v1, 1.0, v1
	v_add_f32_e32 v112, 1.0, v112
	v_add_f32_e32 v135, 1.0, v135
	v_add_f32_e32 v136, 1.0, v136
	v_mul_f32_e32 v113, v115, v113
	v_mul_f32_e32 v115, v121, v131
;     __device__ __forceinline__ void operator()(const f32x4 (&acc)[2][2][4][2], const Unit& u, int wr, int wc, int fr, int fq) const {
;     ...
;         for (int ai = 0; ai < 2; ++ai)
; #pragma unroll
;             for (int m = 0; m < 4; ++m) { const int r = row0 + ai * HALF + m * 16; unsigned char* rowp = O + (size_t)r * ldc + col0;
;                 float sa; if (rowidx) { const int rl = r - cume * BM; sa = (rl < cnte) ? rowmax[u.e * ECAP + rl] : 0.f; } else sa = rowmax[r];
;                 sa *= (1.f / (127.f * 127.f));
;                 float o[8];
; #pragma unroll
;                 for (int n = 0; n < 2; ++n)
; #pragma unroll
;                     for (int j = 0; j < 4; ++j) { const float g = (float)__builtin_bit_cast(i32x4, acc[ai][0][m][n])[j] * (sa * cg[n * 4 + j]), up = (float)__builtin_bit_cast(i32x4, acc[ai][1][m][n])[j] * (sa * cu[n * 4 + j]);
;                         o[n * 4 + j] = g * __builtin_amdgcn_rcpf(1.f + __builtin_amdgcn_exp2f(-1.4426950408889634f * g)) * up; }
;                 u32x2 w; w.x = pack_fp8x4(o[0], o[1], o[2], o[3]); w.y = pack_fp8x4(o[4], o[5], o[6], o[7]);
;                 *(u32x2*)rowp = w; }
	v_mul_f32_e32 v117, v117, v134
	v_rcp_f32_e32 v1, v1
	v_rcp_f32_e32 v112, v112
	v_rcp_f32_e32 v135, v135
	v_rcp_f32_e32 v136, v136
	v_mul_f32_e32 v113, v114, v113
	v_mul_f32_e32 v114, v120, v115
	v_mul_f32_e32 v115, v116, v117
	v_add_f32_e32 v116, 1.0, v137
	v_rcp_f32_e32 v116, v116
	v_mul_f32_e32 v1, v133, v1
	v_mul_f32_e32 v112, v119, v112
	v_mul_f32_e32 v111, v111, v135
	v_mul_f32_e32 v107, v107, v136
	v_mul_f32_e32 v1, v132, v1
	v_mul_f32_e32 v112, v118, v112
	v_mul_f32_e32 v110, v110, v111
	v_mul_f32_e32 v111, v106, v107
	v_mul_f32_e32 v106, v109, v116
	v_mul_f32_e32 v108, v108, v106
	v_med3_f32 v1, v1, s54, v170
	v_med3_f32 v107, v112, s54, v170
	v_mov_b32_e32 v106, 0
	v_cvt_pk_fp8_f32 v106, v1, v107
	v_med3_f32 v1, v115, s54, v170
	v_med3_f32 v110, v110, s54, v170
	v_mov_b32_e32 v107, 0
	v_cvt_pk_fp8_f32 v107, v1, v110
	v_med3_f32 v109, v113, s54, v170
	v_med3_f32 v112, v114, s54, v170
	v_med3_f32 v1, v111, s54, v170
	v_med3_f32 v108, v108, s54, v170
	v_cvt_pk_fp8_f32 v106, v109, v112 op_sel:[0,0,1]
	v_cvt_pk_fp8_f32 v107, v1, v108 op_sel:[0,0,1]
	v_mad_i64_i32 v[108:109], s[26:27], v130, s53, v[158:159]
	v_lshl_add_u64 v[108:109], v[108:109], 0, v[156:157]
	global_store_dwordx2 v[108:109], v[106:107], off
	v_or_b32_e32 v106, 32, v160
	v_ashrrev_i32_e32 v107, 31, v106
	v_lshl_add_u64 v[108:109], v[106:107], 2, s[10:11]
	v_mov_b32_e32 v1, v245
	v_cvt_f32_i32_e32 v109, v102
	v_cvt_f32_i32_e32 v108, v98
	v_cvt_f32_i32_e32 v102, v99
	v_cvt_f32_i32_e32 v99, v104
	v_cvt_f32_i32_e32 v98, v100
	v_cvt_f32_i32_e32 v104, v101
	v_cvt_f32_i32_e32 v101, v94
	v_cvt_f32_i32_e32 v100, v90
	v_cvt_f32_i32_e32 v94, v91
	v_cvt_f32_i32_e32 v91, v96
	v_cvt_f32_i32_e32 v90, v92
	v_cvt_f32_i32_e32 v96, v93
	v_mul_f32_e32 v92, 0x38820610, v1
	v_pk_mul_f32 v[110:111], v[122:123], v[92:93] op_sel_hi:[1,0]
	v_pk_mul_f32 v[112:113], v[70:71], v[92:93] op_sel_hi:[1,0]
	v_pk_mul_f32 v[120:121], v[66:67], v[92:93] op_sel_hi:[1,0]
	v_pk_mul_f32 v[130:131], v[128:129], v[92:93] op_sel_hi:[1,0]
	v_pk_mul_f32 v[114:115], v[124:125], v[92:93] op_sel_hi:[1,0]
	v_pk_mul_f32 v[116:117], v[72:73], v[92:93] op_sel_hi:[1,0]
	v_pk_mul_f32 v[118:119], v[126:127], v[92:93] op_sel_hi:[1,0]
	v_pk_mul_f32 v[92:93], v[68:69], v[92:93] op_sel_hi:[1,0]
	v_pk_mul_f32 v[108:109], v[110:111], v[108:109]
	v_pk_mul_f32 v[102:103], v[112:113], v[102:103]
	v_pk_mul_f32 v[94:95], v[120:121], v[94:95]
	v_pk_mul_f32 v[90:91], v[130:131], v[90:91]
	v_pk_mul_f32 v[98:99], v[114:115], v[98:99]
	v_pk_mul_f32 v[104:105], v[116:117], v[104:105]
	v_pk_mul_f32 v[100:101], v[118:119], v[100:101]
	v_pk_mul_f32 v[92:93], v[92:93], v[96:97]
	v_mul_f32_e32 v1, 0xbfb8aa3b, v109
	v_mul_f32_e32 v96, 0xbfb8aa3b, v103
	v_mul_f32_e32 v111, 0xbfb8aa3b, v95
	v_mul_f32_e32 v112, 0xbfb8aa3b, v91
	v_mul_f32_e32 v97, 0xbfb8aa3b, v99
	v_mul_f32_e32 v107, 0xbfb8aa3b, v105
	v_mul_f32_e32 v110, 0xbfb8aa3b, v101
	v_mul_f32_e32 v113, 0xbfb8aa3b, v93
	v_exp_f32_e32 v1, v1
	v_exp_f32_e32 v96, v96
	v_exp_f32_e32 v111, v111
	v_exp_f32_e32 v112, v112
	v_exp_f32_e32 v97, v97
	v_exp_f32_e32 v107, v107
	v_exp_f32_e32 v110, v110
	v_exp_f32_e32 v113, v113
	v_add_f32_e32 v1, 1.0, v1
	v_add_f32_e32 v96, 1.0, v96
	v_add_f32_e32 v111, 1.0, v111
	v_add_f32_e32 v112, 1.0, v112
	v_add_f32_e32 v97, 1.0, v97
	v_add_f32_e32 v107, 1.0, v107
	v_add_f32_e32 v110, 1.0, v110
	v_add_f32_e32 v113, 1.0, v113
	v_rcp_f32_e32 v1, v1
	v_rcp_f32_e32 v96, v96
	v_rcp_f32_e32 v111, v111
	v_rcp_f32_e32 v112, v112
	v_rcp_f32_e32 v97, v97
	v_rcp_f32_e32 v107, v107
	v_rcp_f32_e32 v110, v110
	v_rcp_f32_e32 v113, v113
	v_mul_f32_e32 v1, v109, v1
	v_mul_f32_e32 v96, v103, v96
	v_mul_f32_e32 v95, v95, v111
	v_mul_f32_e32 v91, v91, v112
	v_mul_f32_e32 v97, v99, v97
	v_mul_f32_e32 v99, v105, v107
	v_mul_f32_e32 v101, v101, v110
	v_mul_f32_e32 v1, v108, v1
	v_mul_f32_e32 v96, v102, v96
	v_mul_f32_e32 v94, v94, v95
	v_mul_f32_e32 v95, v90, v91
	v_mul_f32_e32 v90, v93, v113
	v_mul_f32_e32 v97, v98, v97
	v_mul_f32_e32 v98, v104, v99
	v_mul_f32_e32 v99, v100, v101
	v_mul_f32_e32 v92, v92, v90
	v_med3_f32 v1, v1, s54, v170
	v_med3_f32 v91, v96, s54, v170
	v_mov_b32_e32 v90, 0
	v_cvt_pk_fp8_f32 v90, v1, v91
	v_med3_f32 v1, v99, s54, v170
	v_med3_f32 v94, v94, s54, v170
	v_mov_b32_e32 v91, 0
	v_cvt_pk_fp8_f32 v91, v1, v94
	v_med3_f32 v93, v97, s54, v170
	v_med3_f32 v96, v98, s54, v170
	v_med3_f32 v1, v95, s54, v170
	v_med3_f32 v92, v92, s54, v170
	v_cvt_pk_fp8_f32 v90, v93, v96 op_sel:[0,0,1]
	v_cvt_pk_fp8_f32 v91, v1, v92 op_sel:[0,0,1]
	v_mad_i64_i32 v[92:93], s[26:27], v106, s53, v[158:159]
	v_lshl_add_u64 v[92:93], v[92:93], 0, v[156:157]
	global_store_dwordx2 v[92:93], v[90:91], off
	v_or_b32_e32 v90, 48, v160
	v_ashrrev_i32_e32 v91, 31, v90
	v_lshl_add_u64 v[92:93], v[90:91], 2, s[10:11]
	v_mov_b32_e32 v1, v246
	v_cvt_f32_i32_e32 v93, v86
	v_cvt_f32_i32_e32 v92, v82
	v_cvt_f32_i32_e32 v86, v83
	v_cvt_f32_i32_e32 v83, v88
	v_cvt_f32_i32_e32 v82, v84
	v_cvt_f32_i32_e32 v88, v85
	v_cvt_f32_i32_e32 v85, v78
	v_cvt_f32_i32_e32 v84, v74
	v_cvt_f32_i32_e32 v78, v75
	v_cvt_f32_i32_e32 v75, v80
	v_cvt_f32_i32_e32 v74, v76
	v_cvt_f32_i32_e32 v80, v77
	v_mul_f32_e32 v76, 0x38820610, v1
	v_pk_mul_f32 v[94:95], v[122:123], v[76:77] op_sel_hi:[1,0]
	v_pk_mul_f32 v[96:97], v[70:71], v[76:77] op_sel_hi:[1,0]
	v_pk_mul_f32 v[104:105], v[66:67], v[76:77] op_sel_hi:[1,0]
	v_pk_mul_f32 v[106:107], v[128:129], v[76:77] op_sel_hi:[1,0]
	v_pk_mul_f32 v[98:99], v[124:125], v[76:77] op_sel_hi:[1,0]
	v_pk_mul_f32 v[100:101], v[72:73], v[76:77] op_sel_hi:[1,0]
	v_pk_mul_f32 v[102:103], v[126:127], v[76:77] op_sel_hi:[1,0]
	v_pk_mul_f32 v[76:77], v[68:69], v[76:77] op_sel_hi:[1,0]
;     __device__ __forceinline__ void operator()(const f32x4 (&acc)[2][2][4][2], const Unit& u, int wr, int wc, int fr, int fq) const {
;     ...
;         for (int ai = 0; ai < 2; ++ai)
; #pragma unroll
;             for (int m = 0; m < 4; ++m) { const int r = row0 + ai * HALF + m * 16; unsigned char* rowp = O + (size_t)r * ldc + col0;
;                 float sa; if (rowidx) { const int rl = r - cume * BM; sa = (rl < cnte) ? rowmax[u.e * ECAP + rl] : 0.f; } else sa = rowmax[r];
;                 sa *= (1.f / (127.f * 127.f));
;                 float o[8];
; #pragma unroll
;                 for (int n = 0; n < 2; ++n)
; #pragma unroll
;                     for (int j = 0; j < 4; ++j) { const float g = (float)__builtin_bit_cast(i32x4, acc[ai][0][m][n])[j] * (sa * cg[n * 4 + j]), up = (float)__builtin_bit_cast(i32x4, acc[ai][1][m][n])[j] * (sa * cu[n * 4 + j]);
;                         o[n * 4 + j] = g * __builtin_amdgcn_rcpf(1.f + __builtin_amdgcn_exp2f(-1.4426950408889634f * g)) * up; }
;                 u32x2 w; w.x = pack_fp8x4(o[0], o[1], o[2], o[3]); w.y = pack_fp8x4(o[4], o[5], o[6], o[7]);
;                 *(u32x2*)rowp = w; }
	v_pk_mul_f32 v[92:93], v[94:95], v[92:93]
	v_pk_mul_f32 v[86:87], v[96:97], v[86:87]
	v_pk_mul_f32 v[78:79], v[104:105], v[78:79]
	v_pk_mul_f32 v[74:75], v[106:107], v[74:75]
	v_pk_mul_f32 v[82:83], v[98:99], v[82:83]
	v_pk_mul_f32 v[88:89], v[100:101], v[88:89]
	v_pk_mul_f32 v[84:85], v[102:103], v[84:85]
	v_pk_mul_f32 v[76:77], v[76:77], v[80:81]
	v_mul_f32_e32 v1, 0xbfb8aa3b, v93
	v_mul_f32_e32 v80, 0xbfb8aa3b, v87
	v_mul_f32_e32 v95, 0xbfb8aa3b, v79
	v_mul_f32_e32 v96, 0xbfb8aa3b, v75
	v_mul_f32_e32 v81, 0xbfb8aa3b, v83
	v_mul_f32_e32 v91, 0xbfb8aa3b, v89
	v_mul_f32_e32 v94, 0xbfb8aa3b, v85
	v_mul_f32_e32 v97, 0xbfb8aa3b, v77
	v_exp_f32_e32 v1, v1
	v_exp_f32_e32 v80, v80
	v_exp_f32_e32 v95, v95
	v_exp_f32_e32 v96, v96
	v_exp_f32_e32 v81, v81
	v_exp_f32_e32 v91, v91
	v_exp_f32_e32 v94, v94
	v_exp_f32_e32 v97, v97
	v_add_f32_e32 v1, 1.0, v1
	v_add_f32_e32 v80, 1.0, v80
	v_add_f32_e32 v95, 1.0, v95
	v_add_f32_e32 v96, 1.0, v96
	v_add_f32_e32 v81, 1.0, v81
	v_add_f32_e32 v91, 1.0, v91
	v_add_f32_e32 v94, 1.0, v94
	v_add_f32_e32 v97, 1.0, v97
	v_rcp_f32_e32 v1, v1
	v_rcp_f32_e32 v80, v80
	v_rcp_f32_e32 v95, v95
	v_rcp_f32_e32 v96, v96
	v_rcp_f32_e32 v81, v81
	v_rcp_f32_e32 v91, v91
	v_rcp_f32_e32 v94, v94
	v_rcp_f32_e32 v97, v97
	v_mul_f32_e32 v1, v93, v1
	v_mul_f32_e32 v80, v87, v80
	v_mul_f32_e32 v79, v79, v95
	v_mul_f32_e32 v75, v75, v96
	v_mul_f32_e32 v81, v83, v81
	v_mul_f32_e32 v83, v89, v91
	v_mul_f32_e32 v85, v85, v94
	v_mul_f32_e32 v1, v92, v1
	v_mul_f32_e32 v80, v86, v80
	v_mul_f32_e32 v78, v78, v79
	v_mul_f32_e32 v79, v74, v75
	v_mul_f32_e32 v74, v77, v97
	v_mul_f32_e32 v81, v82, v81
	v_mul_f32_e32 v82, v88, v83
	v_mul_f32_e32 v83, v84, v85
	v_mul_f32_e32 v76, v76, v74
	v_med3_f32 v1, v1, s54, v170
	v_med3_f32 v75, v80, s54, v170
	v_mov_b32_e32 v74, 0
	v_cvt_pk_fp8_f32 v74, v1, v75
	v_med3_f32 v1, v83, s54, v170
	v_med3_f32 v78, v78, s54, v170
	v_mov_b32_e32 v75, 0
	v_cvt_pk_fp8_f32 v75, v1, v78
	v_med3_f32 v77, v81, s54, v170
	v_med3_f32 v80, v82, s54, v170
	v_med3_f32 v1, v79, s54, v170
	v_med3_f32 v76, v76, s54, v170
	v_cvt_pk_fp8_f32 v74, v77, v80 op_sel:[0,0,1]
	v_cvt_pk_fp8_f32 v75, v1, v76 op_sel:[0,0,1]
	v_mad_i64_i32 v[76:77], s[26:27], v90, s53, v[158:159]
	v_lshl_add_u64 v[76:77], v[76:77], 0, v[156:157]
	global_store_dwordx2 v[76:77], v[74:75], off
	v_mov_b32_e32 v1, v247
	v_cvt_f32_i32_e32 v75, v62
	v_cvt_f32_i32_e32 v74, v58
	v_cvt_f32_i32_e32 v62, v59
	v_cvt_f32_i32_e32 v59, v64
	v_cvt_f32_i32_e32 v58, v60
	v_cvt_f32_i32_e32 v64, v61
	v_cvt_f32_i32_e32 v61, v54
	v_cvt_f32_i32_e32 v60, v50
	v_cvt_f32_i32_e32 v54, v51
	v_cvt_f32_i32_e32 v51, v56
	v_cvt_f32_i32_e32 v50, v52
	v_cvt_f32_i32_e32 v56, v53
	v_add_u32_e32 v90, 0x80, v160
	v_mul_f32_e32 v52, 0x38820610, v1
	v_pk_mul_f32 v[76:77], v[122:123], v[52:53] op_sel_hi:[1,0]
	v_pk_mul_f32 v[78:79], v[70:71], v[52:53] op_sel_hi:[1,0]
	v_pk_mul_f32 v[80:81], v[124:125], v[52:53] op_sel_hi:[1,0]
	v_pk_mul_f32 v[82:83], v[72:73], v[52:53] op_sel_hi:[1,0]
	v_pk_mul_f32 v[84:85], v[126:127], v[52:53] op_sel_hi:[1,0]
	v_pk_mul_f32 v[86:87], v[66:67], v[52:53] op_sel_hi:[1,0]
	v_pk_mul_f32 v[88:89], v[128:129], v[52:53] op_sel_hi:[1,0]
	v_pk_mul_f32 v[52:53], v[68:69], v[52:53] op_sel_hi:[1,0]
	v_pk_mul_f32 v[74:75], v[76:77], v[74:75]
	v_pk_mul_f32 v[62:63], v[78:79], v[62:63]
	v_pk_mul_f32 v[58:59], v[80:81], v[58:59]
	v_pk_mul_f32 v[64:65], v[82:83], v[64:65]
	v_pk_mul_f32 v[60:61], v[84:85], v[60:61]
	v_pk_mul_f32 v[54:55], v[86:87], v[54:55]
	v_pk_mul_f32 v[50:51], v[88:89], v[50:51]
	v_pk_mul_f32 v[52:53], v[52:53], v[56:57]
	v_mul_f32_e32 v1, 0xbfb8aa3b, v75
	v_mul_f32_e32 v56, 0xbfb8aa3b, v63
	v_mul_f32_e32 v57, 0xbfb8aa3b, v59
	v_mul_f32_e32 v76, 0xbfb8aa3b, v65
	v_mul_f32_e32 v77, 0xbfb8aa3b, v61
	v_mul_f32_e32 v78, 0xbfb8aa3b, v55
	v_mul_f32_e32 v79, 0xbfb8aa3b, v51
	v_exp_f32_e32 v1, v1
	v_exp_f32_e32 v56, v56
	v_exp_f32_e32 v57, v57
	v_exp_f32_e32 v76, v76
	v_exp_f32_e32 v77, v77
	v_exp_f32_e32 v78, v78
	v_exp_f32_e32 v79, v79
	v_mul_f32_e32 v80, 0xbfb8aa3b, v53
	v_add_f32_e32 v1, 1.0, v1
	v_add_f32_e32 v56, 1.0, v56
	v_exp_f32_e32 v80, v80
	v_add_f32_e32 v57, 1.0, v57
	v_add_f32_e32 v76, 1.0, v76
	v_add_f32_e32 v77, 1.0, v77
	v_add_f32_e32 v78, 1.0, v78
	v_add_f32_e32 v79, 1.0, v79
	v_rcp_f32_e32 v1, v1
	v_rcp_f32_e32 v56, v56
	v_rcp_f32_e32 v57, v57
	v_rcp_f32_e32 v76, v76
	v_rcp_f32_e32 v77, v77
	v_rcp_f32_e32 v78, v78
	v_rcp_f32_e32 v79, v79
	v_add_f32_e32 v80, 1.0, v80
	v_mul_f32_e32 v1, v75, v1
	v_mul_f32_e32 v56, v63, v56
	v_rcp_f32_e32 v80, v80
	v_mul_f32_e32 v57, v59, v57
	v_mul_f32_e32 v59, v65, v76
	v_mul_f32_e32 v61, v61, v77
	v_mul_f32_e32 v55, v55, v78
	v_mul_f32_e32 v51, v51, v79
	v_mul_f32_e32 v1, v74, v1
	v_mul_f32_e32 v56, v62, v56
	v_mul_f32_e32 v57, v58, v57
	v_mul_f32_e32 v58, v64, v59
	v_mul_f32_e32 v59, v60, v61
	v_mul_f32_e32 v54, v54, v55
	v_mul_f32_e32 v55, v50, v51
	v_med3_f32 v1, v1, s54, v170
	v_med3_f32 v51, v56, s54, v170
	v_mov_b32_e32 v50, 0
	v_cvt_pk_fp8_f32 v50, v1, v51
	v_med3_f32 v1, v59, s54, v170
	v_med3_f32 v54, v54, s54, v170
	v_mov_b32_e32 v51, 0
	v_cvt_pk_fp8_f32 v51, v1, v54
	v_mul_f32_e32 v53, v53, v80
	v_mul_f32_e32 v52, v52, v53
	v_med3_f32 v53, v57, s54, v170
	v_med3_f32 v56, v58, s54, v170
	v_med3_f32 v1, v55, s54, v170
	v_med3_f32 v52, v52, s54, v170
	v_cvt_pk_fp8_f32 v50, v53, v56 op_sel:[0,0,1]
	v_cvt_pk_fp8_f32 v51, v1, v52 op_sel:[0,0,1]
	v_mad_i64_i32 v[52:53], s[26:27], v90, s53, v[158:159]
	v_lshl_add_u64 v[52:53], v[52:53], 0, v[156:157]
	global_store_dwordx2 v[52:53], v[50:51], off
	v_mov_b32_e32 v1, v248
	v_cvt_f32_i32_e32 v51, v46
	v_cvt_f32_i32_e32 v50, v42
	v_cvt_f32_i32_e32 v46, v43
;     __device__ __forceinline__ void operator()(const f32x4 (&acc)[2][2][4][2], const Unit& u, int wr, int wc, int fr, int fq) const {
;     ...
;         for (int ai = 0; ai < 2; ++ai)
; #pragma unroll
;             for (int m = 0; m < 4; ++m) { const int r = row0 + ai * HALF + m * 16; unsigned char* rowp = O + (size_t)r * ldc + col0;
;                 float sa; if (rowidx) { const int rl = r - cume * BM; sa = (rl < cnte) ? rowmax[u.e * ECAP + rl] : 0.f; } else sa = rowmax[r];
;                 sa *= (1.f / (127.f * 127.f));
;                 float o[8];
; #pragma unroll
;                 for (int n = 0; n < 2; ++n)
; #pragma unroll
;                     for (int j = 0; j < 4; ++j) { const float g = (float)__builtin_bit_cast(i32x4, acc[ai][0][m][n])[j] * (sa * cg[n * 4 + j]), up = (float)__builtin_bit_cast(i32x4, acc[ai][1][m][n])[j] * (sa * cu[n * 4 + j]);
;                         o[n * 4 + j] = g * __builtin_amdgcn_rcpf(1.f + __builtin_amdgcn_exp2f(-1.4426950408889634f * g)) * up; }
;                 u32x2 w; w.x = pack_fp8x4(o[0], o[1], o[2], o[3]); w.y = pack_fp8x4(o[4], o[5], o[6], o[7]);
;                 *(u32x2*)rowp = w; }
	v_cvt_f32_i32_e32 v43, v48
	v_cvt_f32_i32_e32 v42, v44
	v_cvt_f32_i32_e32 v48, v45
	v_cvt_f32_i32_e32 v45, v38
	v_cvt_f32_i32_e32 v44, v34
	v_cvt_f32_i32_e32 v38, v35
	v_cvt_f32_i32_e32 v35, v40
	v_cvt_f32_i32_e32 v40, v37
	v_cvt_f32_i32_e32 v34, v36
	v_mov_b32_e32 v36, 0
	v_mov_b32_e32 v37, 0
	v_add_u32_e32 v76, 0x90, v160
	v_mul_f32_e32 v52, 0x38820610, v1
	v_pk_mul_f32 v[54:55], v[122:123], v[52:53] op_sel_hi:[1,0]
	v_pk_mul_f32 v[56:57], v[70:71], v[52:53] op_sel_hi:[1,0]
	v_pk_mul_f32 v[58:59], v[124:125], v[52:53] op_sel_hi:[1,0]
	v_pk_mul_f32 v[60:61], v[72:73], v[52:53] op_sel_hi:[1,0]
	v_pk_mul_f32 v[62:63], v[126:127], v[52:53] op_sel_hi:[1,0]
	v_pk_mul_f32 v[64:65], v[66:67], v[52:53] op_sel_hi:[1,0]
	v_pk_mul_f32 v[74:75], v[128:129], v[52:53] op_sel_hi:[1,0]
	v_pk_mul_f32 v[52:53], v[68:69], v[52:53] op_sel_hi:[1,0]
	v_pk_mul_f32 v[50:51], v[54:55], v[50:51]
	v_pk_mul_f32 v[46:47], v[56:57], v[46:47]
	v_pk_mul_f32 v[44:45], v[62:63], v[44:45]
	v_pk_mul_f32 v[38:39], v[64:65], v[38:39]
	v_pk_mul_f32 v[40:41], v[52:53], v[40:41]
	v_mul_f32_e32 v1, 0xbfb8aa3b, v51
	v_mul_f32_e32 v52, 0xbfb8aa3b, v47
	v_mul_f32_e32 v55, 0xbfb8aa3b, v45
	v_mul_f32_e32 v56, 0xbfb8aa3b, v39
	v_exp_f32_e32 v1, v1
	v_exp_f32_e32 v52, v52
	v_exp_f32_e32 v55, v55
	v_exp_f32_e32 v56, v56
	v_pk_mul_f32 v[42:43], v[58:59], v[42:43]
	v_pk_mul_f32 v[48:49], v[60:61], v[48:49]
	v_pk_mul_f32 v[34:35], v[74:75], v[34:35]
	v_mul_f32_e32 v53, 0xbfb8aa3b, v43
	v_mul_f32_e32 v54, 0xbfb8aa3b, v49
	v_mul_f32_e32 v57, 0xbfb8aa3b, v35
	v_mul_f32_e32 v58, 0xbfb8aa3b, v41
	v_add_f32_e32 v1, 1.0, v1
	v_add_f32_e32 v52, 1.0, v52
	v_exp_f32_e32 v53, v53
	v_exp_f32_e32 v54, v54
	v_exp_f32_e32 v57, v57
	v_exp_f32_e32 v58, v58
	v_add_f32_e32 v55, 1.0, v55
	v_add_f32_e32 v56, 1.0, v56
	v_rcp_f32_e32 v1, v1
	v_rcp_f32_e32 v52, v52
	v_rcp_f32_e32 v55, v55
	v_rcp_f32_e32 v56, v56
	v_add_f32_e32 v53, 1.0, v53
	v_add_f32_e32 v54, 1.0, v54
	v_add_f32_e32 v57, 1.0, v57
	v_add_f32_e32 v58, 1.0, v58
	v_mul_f32_e32 v1, v51, v1
	v_mul_f32_e32 v47, v47, v52
	v_rcp_f32_e32 v53, v53
	v_rcp_f32_e32 v54, v54
	v_rcp_f32_e32 v57, v57
	v_rcp_f32_e32 v58, v58
	v_mul_f32_e32 v45, v45, v55
	v_mul_f32_e32 v39, v39, v56
	v_mul_f32_e32 v1, v50, v1
	v_mul_f32_e32 v46, v46, v47
	v_mul_f32_e32 v44, v44, v45
	v_mul_f32_e32 v38, v38, v39
	v_med3_f32 v1, v1, s54, v170
	v_med3_f32 v39, v46, s54, v170
	v_cvt_pk_fp8_f32 v36, v1, v39
	v_med3_f32 v1, v44, s54, v170
	v_med3_f32 v38, v38, s54, v170
	v_cvt_pk_fp8_f32 v37, v1, v38
	v_mul_f32_e32 v43, v43, v53
	v_mul_f32_e32 v49, v49, v54
	v_mul_f32_e32 v35, v35, v57
	v_mul_f32_e32 v41, v41, v58
	v_mul_f32_e32 v42, v42, v43
	v_mul_f32_e32 v43, v48, v49
	v_mul_f32_e32 v34, v34, v35
	v_mul_f32_e32 v35, v40, v41
	v_med3_f32 v40, v42, s54, v170
	v_med3_f32 v41, v43, s54, v170
	v_med3_f32 v1, v34, s54, v170
	v_med3_f32 v34, v35, s54, v170
	v_cvt_pk_fp8_f32 v36, v40, v41 op_sel:[0,0,1]
	v_cvt_pk_fp8_f32 v37, v1, v34 op_sel:[0,0,1]
	v_mad_i64_i32 v[34:35], s[26:27], v76, s53, v[158:159]
	v_lshl_add_u64 v[34:35], v[34:35], 0, v[156:157]
	global_store_dwordx2 v[34:35], v[36:37], off
	v_mov_b32_e32 v1, v249
	v_cvt_f32_i32_e32 v35, v30
	v_cvt_f32_i32_e32 v34, v26
	v_cvt_f32_i32_e32 v30, v27
	v_cvt_f32_i32_e32 v27, v32
	v_cvt_f32_i32_e32 v26, v28
	v_cvt_f32_i32_e32 v32, v29
	v_cvt_f32_i32_e32 v29, v22
	v_cvt_f32_i32_e32 v28, v18
	v_cvt_f32_i32_e32 v22, v19
	v_cvt_f32_i32_e32 v19, v24
	v_cvt_f32_i32_e32 v18, v20
	v_cvt_f32_i32_e32 v24, v21
	v_mov_b32_e32 v20, 0
	v_mov_b32_e32 v21, 0
	v_add_u32_e32 v52, 0xa0, v160
	v_mul_f32_e32 v36, 0x38820610, v1
	v_pk_mul_f32 v[38:39], v[122:123], v[36:37] op_sel_hi:[1,0]
	v_pk_mul_f32 v[40:41], v[70:71], v[36:37] op_sel_hi:[1,0]
	v_pk_mul_f32 v[42:43], v[124:125], v[36:37] op_sel_hi:[1,0]
	v_pk_mul_f32 v[46:47], v[126:127], v[36:37] op_sel_hi:[1,0]
	v_pk_mul_f32 v[48:49], v[66:67], v[36:37] op_sel_hi:[1,0]
	v_pk_mul_f32 v[44:45], v[72:73], v[36:37] op_sel_hi:[1,0]
	v_pk_mul_f32 v[50:51], v[128:129], v[36:37] op_sel_hi:[1,0]
	v_pk_mul_f32 v[36:37], v[68:69], v[36:37] op_sel_hi:[1,0]
	v_pk_mul_f32 v[34:35], v[38:39], v[34:35]
	v_pk_mul_f32 v[30:31], v[40:41], v[30:31]
	v_pk_mul_f32 v[26:27], v[42:43], v[26:27]
	v_pk_mul_f32 v[28:29], v[46:47], v[28:29]
	v_pk_mul_f32 v[22:23], v[48:49], v[22:23]
	v_pk_mul_f32 v[18:19], v[50:51], v[18:19]
	v_pk_mul_f32 v[24:25], v[36:37], v[24:25]
	v_mul_f32_e32 v1, 0xbfb8aa3b, v35
	v_mul_f32_e32 v36, 0xbfb8aa3b, v31
	v_mul_f32_e32 v37, 0xbfb8aa3b, v27
	v_mul_f32_e32 v39, 0xbfb8aa3b, v29
	v_mul_f32_e32 v40, 0xbfb8aa3b, v23
	v_mul_f32_e32 v41, 0xbfb8aa3b, v19
	v_mul_f32_e32 v42, 0xbfb8aa3b, v25
	v_exp_f32_e32 v1, v1
	v_exp_f32_e32 v36, v36
	v_exp_f32_e32 v37, v37
	v_exp_f32_e32 v39, v39
	v_exp_f32_e32 v40, v40
	v_exp_f32_e32 v41, v41
	v_exp_f32_e32 v42, v42
; #define PG8_BAR __builtin_amdgcn_s_barrier()
;     __device__ __forceinline__ void operator()(const f32x4 (&acc)[2][2][4][2], const Unit& u, int wr, int wc, int fr, int fq) const {
;     ...
;             for (int m = 0; m < 4; ++m) { const int r = row0 + ai * HALF + m * 16; unsigned char* rowp = O + (size_t)r * ldc + col0;
;                 float sa; if (rowidx) { const int rl = r - cume * BM; sa = (rl < cnte) ? rowmax[u.e * ECAP + rl] : 0.f; } else sa = rowmax[r];
;                 sa *= (1.f / (127.f * 127.f));
;                 float o[8];
; #pragma unroll
;                 for (int n = 0; n < 2; ++n)
; #pragma unroll
;                     for (int j = 0; j < 4; ++j) { const float g = (float)__builtin_bit_cast(i32x4, acc[ai][0][m][n])[j] * (sa * cg[n * 4 + j]), up = (float)__builtin_bit_cast(i32x4, acc[ai][1][m][n])[j] * (sa * cu[n * 4 + j]);
;                         o[n * 4 + j] = g * __builtin_amdgcn_rcpf(1.f + __builtin_amdgcn_exp2f(-1.4426950408889634f * g)) * up; }
;                 u32x2 w; w.x = pack_fp8x4(o[0], o[1], o[2], o[3]); w.y = pack_fp8x4(o[4], o[5], o[6], o[7]);
;                 *(u32x2*)rowp = w; }
; template <class Epi, class Sched, bool ALIGN_EPI, int DT>
; __device__ __forceinline__ void gemm_phase(LAS unsigned char* lds, const int KB, const Sched& S, const Epi& E) {
;     ...
;         cur = nxt; cB = nB; cA = nA; ++ui;
;         if constexpr (Sched::GATHER) {
; #pragma unroll
;             for (int h = 0; h < 2; ++h)
; #pragma unroll
;                 for (int i = 0; i < 2; ++i) curA[h][i] = nxtA[h][i]; }
;         if constexpr (ALIGN_EPI) { if (wr == 1) PG8_BAR; }
	v_pk_mul_f32 v[32:33], v[44:45], v[32:33]
	v_add_f32_e32 v1, 1.0, v1
	v_mul_f32_e32 v38, 0xbfb8aa3b, v33
	v_exp_f32_e32 v38, v38
	v_add_f32_e32 v36, 1.0, v36
	v_add_f32_e32 v37, 1.0, v37
	v_add_f32_e32 v39, 1.0, v39
	v_add_f32_e32 v40, 1.0, v40
	v_add_f32_e32 v41, 1.0, v41
	v_add_f32_e32 v42, 1.0, v42
	v_rcp_f32_e32 v1, v1
	v_rcp_f32_e32 v36, v36
	v_rcp_f32_e32 v37, v37
	v_rcp_f32_e32 v39, v39
	v_rcp_f32_e32 v40, v40
	v_rcp_f32_e32 v41, v41
	v_rcp_f32_e32 v42, v42
	v_add_f32_e32 v38, 1.0, v38
	v_rcp_f32_e32 v38, v38
	v_mul_f32_e32 v1, v35, v1
	v_mul_f32_e32 v31, v31, v36
	v_mul_f32_e32 v27, v27, v37
	v_mul_f32_e32 v29, v29, v39
	v_mul_f32_e32 v23, v23, v40
	v_mul_f32_e32 v19, v19, v41
	v_mul_f32_e32 v25, v25, v42
	v_mul_f32_e32 v1, v34, v1
	v_mul_f32_e32 v30, v30, v31
	v_mul_f32_e32 v26, v26, v27
	v_mul_f32_e32 v28, v28, v29
	v_mul_f32_e32 v22, v22, v23
	v_mul_f32_e32 v18, v18, v19
	v_mul_f32_e32 v19, v24, v25
	v_med3_f32 v1, v1, s54, v170
	v_med3_f32 v23, v30, s54, v170
	v_med3_f32 v24, v26, s54, v170
	v_med3_f32 v26, v28, s54, v170
	v_med3_f32 v22, v22, s54, v170
	v_cvt_pk_fp8_f32 v20, v1, v23
	v_cvt_pk_fp8_f32 v21, v26, v22
	v_mul_f32_e32 v33, v33, v38
	v_mul_f32_e32 v27, v32, v33
	v_med3_f32 v25, v27, s54, v170
	v_med3_f32 v1, v18, s54, v170
	v_med3_f32 v18, v19, s54, v170
	v_cvt_pk_fp8_f32 v20, v24, v25 op_sel:[0,0,1]
	v_cvt_pk_fp8_f32 v21, v1, v18 op_sel:[0,0,1]
	v_mad_i64_i32 v[18:19], s[26:27], v52, s53, v[158:159]
	v_lshl_add_u64 v[18:19], v[18:19], 0, v[156:157]
	global_store_dwordx2 v[18:19], v[20:21], off
	v_mov_b32_e32 v1, v250
	v_cvt_f32_i32_e32 v19, v6
	v_cvt_f32_i32_e32 v18, v14
	v_cvt_f32_i32_e32 v6, v15
	v_cvt_f32_i32_e32 v15, v8
	v_cvt_f32_i32_e32 v14, v16
	v_cvt_f32_i32_e32 v8, v17
	v_cvt_f32_i32_e32 v17, v2
	v_cvt_f32_i32_e32 v16, v10
	v_cvt_f32_i32_e32 v2, v11
	v_cvt_f32_i32_e32 v11, v4
	v_cvt_f32_i32_e32 v4, v13
	v_cvt_f32_i32_e32 v10, v12
	v_mov_b32_e32 v12, 0
	v_mov_b32_e32 v13, 0
	v_add_u32_e32 v36, 0xb0, v160
	v_mul_f32_e32 v20, 0x38820610, v1
	v_pk_mul_f32 v[22:23], v[122:123], v[20:21] op_sel_hi:[1,0]
	v_pk_mul_f32 v[24:25], v[70:71], v[20:21] op_sel_hi:[1,0]
	v_pk_mul_f32 v[26:27], v[124:125], v[20:21] op_sel_hi:[1,0]
	v_pk_mul_f32 v[28:29], v[72:73], v[20:21] op_sel_hi:[1,0]
	v_pk_mul_f32 v[30:31], v[126:127], v[20:21] op_sel_hi:[1,0]
	v_pk_mul_f32 v[32:33], v[66:67], v[20:21] op_sel_hi:[1,0]
	v_pk_mul_f32 v[34:35], v[128:129], v[20:21] op_sel_hi:[1,0]
	v_pk_mul_f32 v[20:21], v[68:69], v[20:21] op_sel_hi:[1,0]
	v_pk_mul_f32 v[18:19], v[22:23], v[18:19]
	v_pk_mul_f32 v[6:7], v[24:25], v[6:7]
	v_pk_mul_f32 v[14:15], v[26:27], v[14:15]
	v_pk_mul_f32 v[8:9], v[28:29], v[8:9]
	v_pk_mul_f32 v[16:17], v[30:31], v[16:17]
	v_pk_mul_f32 v[2:3], v[32:33], v[2:3]
	v_pk_mul_f32 v[4:5], v[20:21], v[4:5]
	v_mul_f32_e32 v1, 0xbfb8aa3b, v19
	v_mul_f32_e32 v20, 0xbfb8aa3b, v7
	v_mul_f32_e32 v21, 0xbfb8aa3b, v15
	v_mul_f32_e32 v22, 0xbfb8aa3b, v9
	v_mul_f32_e32 v23, 0xbfb8aa3b, v17
	v_mul_f32_e32 v24, 0xbfb8aa3b, v3
	v_mul_f32_e32 v26, 0xbfb8aa3b, v5
	v_exp_f32_e32 v1, v1
	v_exp_f32_e32 v20, v20
	v_exp_f32_e32 v21, v21
	v_exp_f32_e32 v22, v22
	v_exp_f32_e32 v23, v23
	v_exp_f32_e32 v24, v24
	v_exp_f32_e32 v26, v26
	v_pk_mul_f32 v[10:11], v[34:35], v[10:11]
	v_add_f32_e32 v1, 1.0, v1
	v_mul_f32_e32 v25, 0xbfb8aa3b, v11
	v_exp_f32_e32 v25, v25
	v_add_f32_e32 v20, 1.0, v20
	v_add_f32_e32 v21, 1.0, v21
	v_add_f32_e32 v22, 1.0, v22
	v_add_f32_e32 v23, 1.0, v23
	v_add_f32_e32 v24, 1.0, v24
	v_add_f32_e32 v26, 1.0, v26
	v_rcp_f32_e32 v1, v1
	v_rcp_f32_e32 v20, v20
	v_rcp_f32_e32 v21, v21
	v_rcp_f32_e32 v22, v22
	v_rcp_f32_e32 v23, v23
	v_rcp_f32_e32 v24, v24
	v_rcp_f32_e32 v26, v26
	v_add_f32_e32 v25, 1.0, v25
	v_rcp_f32_e32 v25, v25
	v_mul_f32_e32 v1, v19, v1
	v_mul_f32_e32 v7, v7, v20
	v_mul_f32_e32 v15, v15, v21
	v_mul_f32_e32 v9, v9, v22
	v_mul_f32_e32 v17, v17, v23
	v_mul_f32_e32 v3, v3, v24
	v_mul_f32_e32 v5, v5, v26
	v_mul_f32_e32 v1, v18, v1
	v_mul_f32_e32 v6, v6, v7
	v_mul_f32_e32 v7, v14, v15
	v_mul_f32_e32 v8, v8, v9
	v_mul_f32_e32 v9, v16, v17
	v_mul_f32_e32 v2, v2, v3
	v_mul_f32_e32 v4, v4, v5
	v_med3_f32 v1, v1, s54, v170
	v_med3_f32 v5, v6, s54, v170
	v_med3_f32 v6, v7, s54, v170
	v_med3_f32 v7, v8, s54, v170
	v_med3_f32 v8, v9, s54, v170
	v_med3_f32 v2, v2, s54, v170
	v_cvt_pk_fp8_f32 v12, v1, v5
	v_cvt_pk_fp8_f32 v13, v8, v2
	v_mul_f32_e32 v11, v11, v25
	v_mul_f32_e32 v3, v10, v11
	v_med3_f32 v1, v3, s54, v170
	v_med3_f32 v2, v4, s54, v170
	v_cvt_pk_fp8_f32 v12, v6, v7 op_sel:[0,0,1]
	v_cvt_pk_fp8_f32 v13, v1, v2 op_sel:[0,0,1]
	v_mad_i64_i32 v[2:3], s[26:27], v36, s53, v[158:159]
	v_lshl_add_u64 v[2:3], v[2:3], 0, v[156:157]
	global_store_dwordx2 v[2:3], v[12:13], off
	s_cbranch_vccnz .LBB0_1150
	s_andn2_b64 vcc, exec, s[8:9]
	s_cbranch_vccnz .LBB0_1149
	s_nop 0
	s_branch .LBB0_1149
